# v64 + attention K/V row addresses: when the next tile needs no clamping (0 <= MB, MB+31 <= MHI) the 4 addresses are per-lane constants (computed once per pass / unit) plus one scalar offset: 4 VALU in
# baseline (speedup 1.0000x reference)
; #define ATT_LOAD(K_, V_, LR, MB, MHI, RHO) do { _Pragma("unroll") for (int jv = 0; jv < 4; ++jv) { int mv = (MB) + vrow + 8 * jv; mv = max(0, min(mv, (MHI))); \
;                             const unsigned char* rp = ubb + __umul24((unsigned)((mv << (LR)) + (RHO)), (unsigned)(NU * 2)); \
;                             K_[jv] = *(const v4u*)(rp + koff); V_[jv] = *(const v4u*)(rp + voff); } } while (0)
; #define ATT_QLOAD(Q0_, Q1_, OFF, LR) do { const bf16* qp = ub + (size_t)(T0 + (OFF) + ((lane >> 2) << (LR))) * NU + UQ + 8 * (lane & 3); Q0_ = *(const v4u*)qp; Q1_ = *(const v4u*)(qp + 32); } while (0)
; #define ATT_QFRAG(X_) __builtin_bit_cast(bf16x8, lane_perm4((X_), QSRC_LD(lane)))
; template <int layer> __device__ __forceinline__ void layer_phases(const Ctx& c, unsigned char* lds) {
;     ...
;                     int s = 0, j = 0, lr, rho, m0, off, base, ni; ATT_BLOCK(0, lr, rho, m0, off, base, ni);
;                     bf16x8 qf0, qf1; v4u qn0, qn1; ATT_QLOAD(qn0, qn1, off, lr);
;                     v4u ka[4], kb[4], va_[4], vb_[4];
;                     ATT_LOAD(ka, va_, lr, base + 128, m0 + 15, rho);
;                     asm volatile("" ::: "memory");
;                     __syncthreads();
; #pragma unroll
;                     for (int q = 0; q < 2; ++q) { const int i4 = tid + NTHR * q; if (i4 < 864) ((f32x4*)LUTl)[i4] = bq[q]; }
;                     __syncthreads();
;                     qf0 = ATT_QFRAG(qn0); qf1 = ATT_QFRAG(qn1);
;                     float m_ref = -INFINITY, l_run = 0.f; f32x4 o[4];
; #pragma unroll
;                     for (int d = 0; d < 4; ++d) o[d] = (f32x4){0.f, 0.f, 0.f, 0.f};
;                     bool done = false; (void)rho;
.LBB0_417:
	s_or_b64 exec, exec, s[22:23]
	s_sub_i32 s22, 0x80, s39
	s_waitcnt vmcnt(9)
	ds_bpermute_b32 v14, v147, v6
	ds_bpermute_b32 v15, v147, v7
	ds_bpermute_b32 v16, v147, v8
	ds_bpermute_b32 v17, v147, v9
	s_waitcnt vmcnt(8)
	ds_bpermute_b32 v18, v147, v10
	ds_bpermute_b32 v19, v147, v11
	ds_bpermute_b32 v20, v147, v12
	ds_bpermute_b32 v21, v147, v13
	s_ashr_i32 s22, s22, 5
	s_ashr_i32 s19, s18, 31
	s_lshl_b32 s14, s14, 6
	s_sub_i32 s22, 5, s22
	v_mov_b32_e32 v4, v2
	v_mov_b32_e32 v5, v2
	s_cmpk_lt_i32 s39, 0x80
	v_mov_b32_e32 v123, v2
	v_mov_b32_e32 v3, v2
	v_mov_b64_e32 v[56:57], v[4:5]
	v_mov_b64_e32 v[60:61], v[4:5]
	v_mov_b64_e32 v[64:65], v[4:5]
	v_mov_b64_e32 v[68:69], v[4:5]
	s_cselect_b32 s22, s22, 5
	v_lshl_add_u64 v[126:127], s[20:21], 0, v[122:123]
	v_lshl_add_u64 v[128:129], s[20:21], 0, v[118:119]
	s_mov_b32 s35, 0
	v_mov_b32_e32 v130, 0xff800000
	v_mov_b32_e32 v131, 0
	v_mov_b64_e32 v[54:55], v[2:3]
	v_mov_b64_e32 v[58:59], v[2:3]
	v_mov_b64_e32 v[62:63], v[2:3]
	v_mov_b64_e32 v[66:67], v[2:3]
	s_mov_b32 s36, s2
	s_mov_b32 s34, 0
	s_waitcnt lgkmcnt(0)
	s_barrier
	v_lshlrev_b32_e32 v172, 4, v142
	v_mul_u32_u24_e32 v172, 0x1800, v172
	v_mov_b32_e32 v173, 0
	v_lshl_add_u64 v[174:175], v[128:129], 0, v[172:173]
	v_or_b32_e32 v172, 8, v142
	v_lshlrev_b32_e32 v172, 4, v172
	v_mul_u32_u24_e32 v172, 0x1800, v172
	v_mov_b32_e32 v173, 0
	v_lshl_add_u64 v[176:177], v[128:129], 0, v[172:173]
	v_or_b32_e32 v172, 16, v142
	v_lshlrev_b32_e32 v172, 4, v172
	v_mul_u32_u24_e32 v172, 0x1800, v172
	v_mov_b32_e32 v173, 0
	v_lshl_add_u64 v[178:179], v[128:129], 0, v[172:173]
	v_or_b32_e32 v172, 24, v142
	v_lshlrev_b32_e32 v172, 4, v172
	v_mul_u32_u24_e32 v172, 0x1800, v172
	v_mov_b32_e32 v173, 0
	v_lshl_add_u64 v[180:181], v[128:129], 0, v[172:173]
	s_branch .LBB0_421

.LBB0_421:
	s_add_i32 s23, s35, 1
	s_cmp_ge_i32 s23, s22
	s_cselect_b64 s[20:21], -1, 0
	s_and_b64 s[24:25], s[20:21], exec
	s_cselect_b32 s25, 0, s23
	s_cmp_lg_u64 s[20:21], 0
	s_addc_u32 s37, s34, 0
	s_cmp_lt_i32 s37, 2
	s_cselect_b64 s[20:21], -1, 0
	s_cmp_gt_i32 s37, 1
	s_cselect_b32 s24, s34, s37
	s_cselect_b32 s57, s35, s25
	s_add_i32 s24, s24, s2
	s_add_i32 s23, s24, s31
	s_ashr_i32 s49, s23, 4
	s_and_b32 s48, s49, 0xffffffe0
	s_lshl_b32 s56, s57, 5
	s_sub_i32 s58, s48, s56
	s_cmp_lt_i32 s58, 0
	s_cbranch_scc1 .Latt0_slow4
	s_add_i32 s98, s58, 31
	s_add_i32 s99, s49, 15
	s_cmp_gt_i32 s98, s99
	s_cbranch_scc1 .Latt0_slow4
	s_lshl_b32 s98, s58, 4
	s_add_i32 s98, s98, s24
	s_mulk_i32 s98, 0x1800
	s_mov_b32 s99, 0
	v_lshl_add_u64 v[4:5], s[98:99], 0, v[174:175]
	global_load_dwordx4 v[78:81], v[4:5], off offset:512
	global_load_dwordx4 v[70:73], v[4:5], off offset:1024
	v_lshl_add_u64 v[4:5], s[98:99], 0, v[176:177]
	global_load_dwordx4 v[86:89], v[4:5], off offset:512
	global_load_dwordx4 v[74:77], v[4:5], off offset:1024
	v_lshl_add_u64 v[4:5], s[98:99], 0, v[178:179]
	global_load_dwordx4 v[94:97], v[4:5], off offset:512
	global_load_dwordx4 v[82:85], v[4:5], off offset:1024
	v_lshl_add_u64 v[4:5], s[98:99], 0, v[180:181]
	global_load_dwordx4 v[98:101], v[4:5], off offset:512
	global_load_dwordx4 v[90:93], v[4:5], off offset:1024
	s_add_i32 s58, s49, 15
	s_branch .Latt0_join4
.Latt0_slow4:
	v_or_b32_e32 v1, s58, v142
	s_add_i32 s58, s49, 15
	v_min_i32_e32 v3, s58, v1
	v_max_i32_e32 v3, 0, v3
	v_lshl_add_u32 v3, v3, 4, s24
	v_mul_u32_u24_e32 v4, 0x1800, v3
	v_or_b32_e32 v3, 8, v1
	v_min_i32_e32 v3, s58, v3
	v_ashrrev_i32_e32 v5, 31, v4
	v_max_i32_e32 v3, 0, v3
	v_lshl_add_u64 v[4:5], v[128:129], 0, v[4:5]
	v_lshl_add_u32 v3, v3, 4, s24
	global_load_dwordx4 v[78:81], v[4:5], off offset:512
	global_load_dwordx4 v[70:73], v[4:5], off offset:1024
	v_mul_u32_u24_e32 v4, 0x1800, v3
	v_or_b32_e32 v3, 16, v1
	v_min_i32_e32 v3, s58, v3
	v_ashrrev_i32_e32 v5, 31, v4
	v_max_i32_e32 v3, 0, v3
	v_lshl_add_u64 v[4:5], v[128:129], 0, v[4:5]
	v_lshl_add_u32 v3, v3, 4, s24
	v_or_b32_e32 v1, 24, v1
	global_load_dwordx4 v[86:89], v[4:5], off offset:512
	global_load_dwordx4 v[74:77], v[4:5], off offset:1024
	v_mul_u32_u24_e32 v4, 0x1800, v3
	v_min_i32_e32 v1, s58, v1
	v_ashrrev_i32_e32 v5, 31, v4
	v_max_i32_e32 v1, 0, v1
	v_lshl_add_u64 v[4:5], v[128:129], 0, v[4:5]
	v_lshl_add_u32 v1, v1, 4, s24
	global_load_dwordx4 v[94:97], v[4:5], off offset:512
	global_load_dwordx4 v[82:85], v[4:5], off offset:1024
	v_mul_u32_u24_e32 v4, 0x1800, v1
	v_ashrrev_i32_e32 v5, 31, v4
	v_lshl_add_u64 v[4:5], v[128:129], 0, v[4:5]
	global_load_dwordx4 v[98:101], v[4:5], off offset:512
	global_load_dwordx4 v[90:93], v[4:5], off offset:1024
.Latt0_join4:
	s_cmp_lg_u32 s57, 0
	s_cbranch_scc1 .LBB0_423
	v_add_u32_e32 v1, s23, v144
	v_mad_i64_i32 v[4:5], s[58:59], v1, s27, v[126:127]
	global_load_dwordx4 v[6:9], v[4:5], off
	global_load_dwordx4 v[10:13], v[4:5], off offset:64

.LBB0_431:
	s_andn2_b64 vcc, exec, s[20:21]
	s_mov_b64 s[20:21], -1
	s_cbranch_vccnz .LBB0_420
	s_sub_i32 s20, 0x80, s48
	s_ashr_i32 s20, s20, 5
	s_sub_i32 s20, 5, s20
	s_cmpk_lt_i32 s48, 0x80
	s_cselect_b32 s57, s20, 5
	s_add_i32 s34, s25, 1
	s_cmp_ge_i32 s34, s57
	s_cselect_b64 s[20:21], -1, 0
	s_and_b64 s[22:23], s[20:21], exec
	s_cselect_b32 s35, 0, s34
	s_cmp_lg_u64 s[20:21], 0
	s_addc_u32 s34, s37, 0
	s_cmp_lt_i32 s34, 2
	s_cselect_b64 s[22:23], -1, 0
	s_cmp_gt_i32 s34, 1
	s_cselect_b64 s[20:21], -1, 0
	s_and_b64 s[38:39], s[20:21], exec
	s_cselect_b32 s36, s37, s34
	s_cselect_b32 s59, s25, s35
	s_add_i32 s36, s36, s2
	s_add_i32 s58, s36, s31
	s_ashr_i32 s38, s58, 4
	s_and_b32 s39, s38, 0xffffffe0
	s_lshl_b32 s60, s59, 5
	s_sub_i32 s60, s39, s60
	s_cmp_lt_i32 s60, 0
	s_cbranch_scc1 .Latt0_slow3
	s_add_i32 s98, s60, 31
	s_add_i32 s99, s38, 15
	s_cmp_gt_i32 s98, s99
	s_cbranch_scc1 .Latt0_slow3
	s_lshl_b32 s98, s60, 4
	s_add_i32 s98, s98, s36
	s_mulk_i32 s98, 0x1800
	s_mov_b32 s99, 0
	v_lshl_add_u64 v[4:5], s[98:99], 0, v[174:175]
	global_load_dwordx4 v[26:29], v[4:5], off offset:512
	global_load_dwordx4 v[22:25], v[4:5], off offset:1024
	v_lshl_add_u64 v[4:5], s[98:99], 0, v[176:177]
	global_load_dwordx4 v[34:37], v[4:5], off offset:512
	global_load_dwordx4 v[30:33], v[4:5], off offset:1024
	v_lshl_add_u64 v[4:5], s[98:99], 0, v[178:179]
	global_load_dwordx4 v[42:45], v[4:5], off offset:512
	global_load_dwordx4 v[38:41], v[4:5], off offset:1024
	v_lshl_add_u64 v[4:5], s[98:99], 0, v[180:181]
	global_load_dwordx4 v[50:53], v[4:5], off offset:512
	global_load_dwordx4 v[46:49], v[4:5], off offset:1024
	s_add_i32 s60, s38, 15
	s_branch .Latt0_join3
.Latt0_slow3:
	v_or_b32_e32 v1, s60, v142
	s_add_i32 s60, s38, 15
	v_min_i32_e32 v3, s60, v1
	v_max_i32_e32 v3, 0, v3
	v_lshl_add_u32 v3, v3, 4, s36
	v_mul_u32_u24_e32 v4, 0x1800, v3
	v_or_b32_e32 v3, 8, v1
	v_min_i32_e32 v3, s60, v3
	v_ashrrev_i32_e32 v5, 31, v4
	v_max_i32_e32 v3, 0, v3
	v_lshl_add_u64 v[4:5], v[128:129], 0, v[4:5]
	v_lshl_add_u32 v3, v3, 4, s36
	global_load_dwordx4 v[26:29], v[4:5], off offset:512
	global_load_dwordx4 v[22:25], v[4:5], off offset:1024
	v_mul_u32_u24_e32 v4, 0x1800, v3
	v_or_b32_e32 v3, 16, v1
	v_min_i32_e32 v3, s60, v3
	v_ashrrev_i32_e32 v5, 31, v4
	v_max_i32_e32 v3, 0, v3
	v_lshl_add_u64 v[4:5], v[128:129], 0, v[4:5]
	v_lshl_add_u32 v3, v3, 4, s36
	v_or_b32_e32 v1, 24, v1
	global_load_dwordx4 v[34:37], v[4:5], off offset:512
	global_load_dwordx4 v[30:33], v[4:5], off offset:1024
	v_mul_u32_u24_e32 v4, 0x1800, v3
	v_min_i32_e32 v1, s60, v1
	v_ashrrev_i32_e32 v5, 31, v4
	v_max_i32_e32 v1, 0, v1
	v_lshl_add_u64 v[4:5], v[128:129], 0, v[4:5]
	v_lshl_add_u32 v1, v1, 4, s36
	global_load_dwordx4 v[42:45], v[4:5], off offset:512
	global_load_dwordx4 v[38:41], v[4:5], off offset:1024
	v_mul_u32_u24_e32 v4, 0x1800, v1
	v_ashrrev_i32_e32 v5, 31, v4
	v_lshl_add_u64 v[4:5], v[128:129], 0, v[4:5]
	global_load_dwordx4 v[50:53], v[4:5], off offset:512
	global_load_dwordx4 v[46:49], v[4:5], off offset:1024
.Latt0_join3:
	s_cmp_lg_u32 s59, 0
	s_cbranch_scc1 .LBB0_434
	v_add_u32_e32 v1, s58, v144
	v_mad_i64_i32 v[4:5], s[58:59], v1, s27, v[126:127]
	global_load_dwordx4 v[6:9], v[4:5], off
	global_load_dwordx4 v[10:13], v[4:5], off offset:64

; #define ATT_LOAD(K_, V_, LR, MB, MHI, RHO) do { _Pragma("unroll") for (int jv = 0; jv < 4; ++jv) { int mv = (MB) + vrow + 8 * jv; mv = max(0, min(mv, (MHI))); \
;                             const unsigned char* rp = ubb + __umul24((unsigned)((mv << (LR)) + (RHO)), (unsigned)(NU * 2)); \
;                             K_[jv] = *(const v4u*)(rp + koff); V_[jv] = *(const v4u*)(rp + voff); } } while (0)
; #define ATT_QLOAD(Q0_, Q1_, OFF, LR) do { const bf16* qp = ub + (size_t)(T0 + (OFF) + ((lane >> 2) << (LR))) * NU + UQ + 8 * (lane & 3); Q0_ = *(const v4u*)qp; Q1_ = *(const v4u*)(qp + 32); } while (0)
; #define ATT_QFRAG(X_) __builtin_bit_cast(bf16x8, lane_perm4((X_), QSRC_LD(lane)))
; template <int layer> __device__ __forceinline__ void layer_phases(const Ctx& c, unsigned char* lds) {
;     ...
;                     for (int p = 1; p <= 2; ++p) {
;                         const int lr = 4 - 2 * p; const int offA = (p == 1) ? 128 * (wv >> 2) + (wv & 3) : 32 * wv, rho = (p == 1) ? (wv & 3) : 0; const int offB = offA + (16 << lr);
;                         const int m0A = (T0 + offA) >> lr, mhiB = m0A + 31; const int base = (m0A - 128) & ~31, top = mhiB & ~31; const int pz = (base < 0) ? ((-base) >> 5) : 0; const int ni = ((top - base) >> 5) + 1 - pz;
;                         v4u qa0, qa1, qb0_, qb1_; ATT_QLOAD(qa0, qa1, offA, lr); ATT_QLOAD(qb0_, qb1_, offB, lr);
;                         ATT_LOAD(ka, va_, lr, top, mhiB, rho);
;                         asm volatile("" ::: "memory");
;                         __syncthreads();
;                         bf16x8 qx[2][2]; qx[0][0] = ATT_QFRAG(qa0); qx[0][1] = ATT_QFRAG(qa1); qx[1][0] = ATT_QFRAG(qb0_); qx[1][1] = ATT_QFRAG(qb1_);
;                         float mx[2], lx[2]; f32x4 ox[2][4];
; #pragma unroll
;                         for (int bk = 0; bk < 2; ++bk) { const int qi = (bk ? offB : offA) + (ql << lr); const float* sp = STl + (qi ^ (qi >> 4)) * 68 + 4 * g4;
; #pragma unroll
;                             for (int d = 0; d < 4; ++d) ox[bk][d] = *(const f32x4*)(sp + 16 * d);
;                             mx[bk] = sp[64 - 4 * g4]; lx[bk] = (g4 == 0) ? sp[65] : 0.f; }
;                         int j = 0;
.LBB0_448:
	s_lshl_b32 s14, s37, 1
	s_sub_i32 s14, 4, s14
	s_and_b64 s[20:21], s[22:23], exec
	s_cselect_b32 s36, s26, s16
	s_cselect_b32 s21, s3, 0
	s_add_i32 s24, s36, s31
	v_lshlrev_b32_e32 v1, s14, v143
	s_lshl_b32 s20, 16, s14
	v_add_u32_e32 v3, s24, v1
	s_add_i32 s20, s20, s36
	s_ashr_i32 s38, s24, s14
	s_waitcnt vmcnt(1)
	v_mad_i64_i32 v[8:9], s[24:25], v3, s27, v[126:127]
	s_add_i32 s34, s38, 31
	s_add_i32 s24, s20, s31
	s_and_b32 s35, s34, 0xffffffe0
	v_add_u32_e32 v1, s24, v1
	s_waitcnt lgkmcnt(4)
	v_mad_i64_i32 v[16:17], s[24:25], v1, s27, v[126:127]
	v_or_b32_e32 v1, s35, v142
	v_min_i32_e32 v3, s34, v1
	v_max_i32_e32 v3, 0, v3
	v_lshlrev_b32_e32 v3, s14, v3
	v_add_u32_e32 v3, s21, v3
	s_waitcnt lgkmcnt(1)
	v_mul_u32_u24_e32 v20, 0x1800, v3
	v_or_b32_e32 v3, 8, v1
	v_min_i32_e32 v3, s34, v3
	v_max_i32_e32 v3, 0, v3
	s_waitcnt lgkmcnt(0)
	v_ashrrev_i32_e32 v21, 31, v20
	v_lshlrev_b32_e32 v3, s14, v3
	v_lshl_add_u64 v[20:21], v[128:129], 0, v[20:21]
	v_add_u32_e32 v3, s21, v3
	global_load_dwordx4 v[4:7], v[8:9], off
	s_nop 0
	global_load_dwordx4 v[8:11], v[8:9], off offset:64
	s_nop 0
	global_load_dwordx4 v[12:15], v[16:17], off
	s_nop 0
	global_load_dwordx4 v[16:19], v[16:17], off offset:64
	s_nop 0
	global_load_dwordx4 v[56:59], v[20:21], off offset:512
	global_load_dwordx4 v[52:55], v[20:21], off offset:1024
	v_mul_u32_u24_e32 v20, 0x1800, v3
	v_or_b32_e32 v3, 16, v1
	v_min_i32_e32 v3, s34, v3
	v_max_i32_e32 v3, 0, v3
	v_ashrrev_i32_e32 v21, 31, v20
	v_lshlrev_b32_e32 v3, s14, v3
	v_or_b32_e32 v1, 24, v1
	v_lshl_add_u64 v[20:21], v[128:129], 0, v[20:21]
	v_add_u32_e32 v3, s21, v3
	v_min_i32_e32 v1, s34, v1
	global_load_dwordx4 v[64:67], v[20:21], off offset:512
	global_load_dwordx4 v[60:63], v[20:21], off offset:1024
	v_mul_u32_u24_e32 v20, 0x1800, v3
	v_max_i32_e32 v1, 0, v1
	v_ashrrev_i32_e32 v21, 31, v20
	v_lshlrev_b32_e32 v1, s14, v1
	v_lshl_add_u64 v[20:21], v[128:129], 0, v[20:21]
	v_add_u32_e32 v1, s21, v1
	global_load_dwordx4 v[72:75], v[20:21], off offset:512
	global_load_dwordx4 v[68:71], v[20:21], off offset:1024
	v_mul_u32_u24_e32 v20, 0x1800, v1
	v_ashrrev_i32_e32 v21, 31, v20
	v_lshl_add_u64 v[20:21], v[128:129], 0, v[20:21]
	global_load_dwordx4 v[80:83], v[20:21], off offset:512
	global_load_dwordx4 v[76:79], v[20:21], off offset:1024
	v_lshlrev_b32_e32 v3, s14, v141
	v_add_u32_e32 v1, s36, v3
	v_lshrrev_b32_e32 v20, 4, v1
	v_xor_b32_e32 v1, v20, v1
	v_mul_lo_u32 v123, v1, s29
	v_add_u32_e32 v1, 0, v123
	s_barrier
	v_mov_b32_e32 v138, 0
	s_waitcnt vmcnt(11)
	ds_bpermute_b32 v36, v147, v4
	v_lshl_add_u32 v4, v146, 2, v1
	ds_read_b128 v[32:35], v4 offset:14336
	ds_read_b128 v[28:31], v4 offset:14400
	ds_read_b128 v[24:27], v4 offset:14464
	ds_read_b128 v[20:23], v4 offset:14528
	ds_read_b32 v136, v1 offset:14592
	ds_bpermute_b32 v37, v147, v5
	ds_bpermute_b32 v38, v147, v6
	ds_bpermute_b32 v39, v147, v7
	s_waitcnt vmcnt(10)
	ds_bpermute_b32 v40, v147, v8
	ds_bpermute_b32 v41, v147, v9
	ds_bpermute_b32 v42, v147, v10
	ds_bpermute_b32 v43, v147, v11
	s_waitcnt vmcnt(9)
	ds_bpermute_b32 v44, v147, v12
	ds_bpermute_b32 v45, v147, v13
	ds_bpermute_b32 v46, v147, v14
	ds_bpermute_b32 v47, v147, v15
	s_waitcnt vmcnt(8)
	ds_bpermute_b32 v48, v147, v16
	ds_bpermute_b32 v49, v147, v17
	ds_bpermute_b32 v50, v147, v18
	ds_bpermute_b32 v51, v147, v19
	v_mov_b32_e32 v1, 0
	s_and_saveexec_b64 s[24:25], s[4:5]
	ds_read_b32 v138, v4 offset:14596
	s_or_b64 exec, exec, s[24:25]
	v_add_u32_e32 v3, s20, v3
	v_lshrrev_b32_e32 v4, 4, v3
	v_xor_b32_e32 v3, v4, v3
	v_mul_lo_u32 v3, v3, s29
	v_add_u32_e32 v85, 0, v3
	v_lshl_add_u32 v84, v146, 2, v85
	ds_read_b128 v[16:19], v84 offset:14336
	ds_read_b128 v[12:15], v84 offset:14400
	ds_read_b128 v[8:11], v84 offset:14464
	ds_read_b128 v[4:7], v84 offset:14528
	ds_read_b32 v134, v85 offset:14592
	s_and_saveexec_b64 s[24:25], s[4:5]
	ds_read_b32 v1, v84 offset:14596
	s_or_b64 exec, exec, s[24:25]
	s_and_b32 s24, s38, 0xffffffe0
	s_and_b32 s36, s38, 31
	s_sub_i32 s25, 0x80, s24
	s_addk_i32 s36, 0x9f
	s_xor_b64 s[22:23], s[22:23], -1
	s_ashr_i32 s25, s25, 5
	s_lshr_b32 s36, s36, 5
	s_cmpk_lt_i32 s24, 0x80
	s_cselect_b32 s24, s25, 0
	s_sub_i32 s36, s36, s24
	s_mul_i32 s24, s37, 0x1200
	s_lshl_b32 s25, s38, 2
	s_add_i32 s24, s24, s25
	s_lshl_b32 s25, s34, 2
	s_and_b32 s25, s25, 0xffffff80
	s_sub_i32 s24, s24, s25
	s_add_i32 s36, s36, 1
	s_mov_b32 s37, 2
	v_add_u32_e32 v135, s24, v154
	v_lshlrev_b32_e32 v172, s14, v142
	v_mul_u32_u24_e32 v172, 0x1800, v172
	v_mov_b32_e32 v173, 0
	v_lshl_add_u64 v[164:165], v[128:129], 0, v[172:173]
	v_or_b32_e32 v172, 8, v142
	v_lshlrev_b32_e32 v172, s14, v172
	v_mul_u32_u24_e32 v172, 0x1800, v172
	v_mov_b32_e32 v173, 0
	v_lshl_add_u64 v[166:167], v[128:129], 0, v[172:173]
	v_or_b32_e32 v172, 16, v142
	v_lshlrev_b32_e32 v172, s14, v172
	v_mul_u32_u24_e32 v172, 0x1800, v172
	v_mov_b32_e32 v173, 0
	v_lshl_add_u64 v[168:169], v[128:129], 0, v[172:173]
	v_or_b32_e32 v172, 24, v142
	v_lshlrev_b32_e32 v172, s14, v172
	v_mul_u32_u24_e32 v172, 0x1800, v172
	v_mov_b32_e32 v173, 0
	v_lshl_add_u64 v[170:171], v[128:129], 0, v[172:173]
	s_branch .LBB0_454

.LBB0_454:
	s_add_i32 s39, s37, -2
	s_add_i32 s38, s37, -1
	s_cmp_lt_i32 s38, s36
	s_cselect_b64 s[24:25], -1, 0
	s_and_b64 s[48:49], s[24:25], exec
	s_cselect_b32 s39, s38, s39
	s_lshl_b32 s39, s39, 5
	s_sub_i32 s39, s35, s39
	s_waitcnt vmcnt(0)
	s_cmp_lt_i32 s39, 0
	s_cbranch_scc1 .Latt_slow3
	s_add_i32 s98, s39, 31
	s_cmp_gt_i32 s98, s34
	s_cbranch_scc1 .Latt_slow3
	s_lshl_b32 s98, s39, s14
	s_add_i32 s98, s98, s21
	s_mulk_i32 s98, 0x1800
	s_mov_b32 s99, 0
	v_lshl_add_u64 v[84:85], s[98:99], 0, v[164:165]
	v_lshl_add_u64 v[88:89], s[98:99], 0, v[166:167]
	v_lshl_add_u64 v[96:97], s[98:99], 0, v[168:169]
	v_lshl_add_u64 v[104:105], s[98:99], 0, v[170:171]
	s_branch .Latt_join3
.Latt_slow3:
	v_or_b32_e32 v104, s39, v142
	v_min_i32_e32 v84, s34, v104
	v_or_b32_e32 v88, 8, v104
	v_or_b32_e32 v96, 16, v104
	v_or_b32_e32 v104, 24, v104
	v_min_i32_e32 v88, s34, v88
	v_min_i32_e32 v96, s34, v96
	v_min_i32_e32 v104, s34, v104
	v_max_i32_e32 v84, 0, v84
	v_max_i32_e32 v88, 0, v88
	v_max_i32_e32 v96, 0, v96
	v_max_i32_e32 v104, 0, v104
	v_lshlrev_b32_e32 v84, s14, v84
	v_lshlrev_b32_e32 v88, s14, v88
	v_lshlrev_b32_e32 v96, s14, v96
	v_lshlrev_b32_e32 v104, s14, v104
	v_add_u32_e32 v84, s21, v84
	v_add_u32_e32 v88, s21, v88
	v_add_u32_e32 v96, s21, v96
	v_add_u32_e32 v104, s21, v104
	v_mul_u32_u24_e32 v84, 0x1800, v84
	v_mul_u32_u24_e32 v88, 0x1800, v88
	v_mul_u32_u24_e32 v96, 0x1800, v96
	v_mul_u32_u24_e32 v104, 0x1800, v104
	v_ashrrev_i32_e32 v85, 31, v84
	v_ashrrev_i32_e32 v89, 31, v88
	v_ashrrev_i32_e32 v97, 31, v96
	v_ashrrev_i32_e32 v105, 31, v104
	v_lshl_add_u64 v[84:85], v[128:129], 0, v[84:85]
	v_lshl_add_u64 v[88:89], v[128:129], 0, v[88:89]
	v_lshl_add_u64 v[96:97], v[128:129], 0, v[96:97]
	v_lshl_add_u64 v[104:105], v[128:129], 0, v[104:105]
.Latt_join3:
	global_load_dwordx4 v[92:95], v[84:85], off offset:512
	s_nop 0
	global_load_dwordx4 v[84:87], v[84:85], off offset:1024
	s_nop 0
	global_load_dwordx4 v[100:103], v[88:89], off offset:512
	s_nop 0
	global_load_dwordx4 v[88:91], v[88:89], off offset:1024
	s_nop 0
	global_load_dwordx4 v[108:111], v[96:97], off offset:512
	s_nop 0
	global_load_dwordx4 v[96:99], v[96:97], off offset:1024
	s_nop 0
	global_load_dwordx4 v[112:115], v[104:105], off offset:512
	s_nop 0
	global_load_dwordx4 v[104:107], v[104:105], off offset:1024
	s_waitcnt vmcnt(15)
	ds_write_b128 v155, v[56:59]
	s_waitcnt vmcnt(13)
	ds_write_b128 v155, v[64:67] offset:1152
	s_waitcnt vmcnt(11)
	ds_write_b128 v155, v[72:75] offset:2304
	s_waitcnt vmcnt(9)
	ds_write_b128 v155, v[80:83] offset:3456
	ds_read_b128 v[56:59], v156 offset:2368
	ds_read_b128 v[64:67], v156 offset:2304
	ds_read_b128 v[72:75], v156 offset:64
	ds_read_b128 v[80:83], v156
	s_waitcnt lgkmcnt(0)
	ds_write_b128 v157, v[52:55]
	ds_write_b128 v157, v[60:63] offset:1280
	ds_write_b128 v157, v[68:71] offset:2560
	s_waitcnt vmcnt(8)
	ds_write_b128 v157, v[76:79] offset:3840
	v_mfma_f32_16x16x32_bf16 v[52:55], v[80:83], v[36:39], 0
	ds_read2_b32 v[68:69], v135 offset0:18 offset1:19
	ds_read2_b32 v[70:71], v135 offset0:16 offset1:17
	ds_read2_b32 v[76:77], v135 offset0:2 offset1:3
	ds_read2_b32 v[78:79], v135 offset1:1
	s_waitcnt lgkmcnt(0)
	v_mfma_f32_16x16x32_bf16 v[60:63], v[64:67], v[36:39], 0
	v_mfma_f32_16x16x32_bf16 v[52:55], v[72:75], v[40:43], v[52:55]
	v_mfma_f32_16x16x32_bf16 v[60:63], v[56:59], v[40:43], v[60:63]
	s_nop 6
	v_add_f32_e32 v52, v52, v69
	v_add_f32_e32 v53, v53, v68
	v_max3_f32 v68, v52, s28, v53
	v_add_f32_e32 v54, v54, v71
	v_add_f32_e32 v55, v55, v70
	v_max3_f32 v68, v68, v54, v55
	v_add_f32_e32 v60, v60, v77
	v_add_f32_e32 v61, v61, v76
	v_max3_f32 v68, v68, v60, v61
	v_add_f32_e32 v62, v62, v79
	v_add_f32_e32 v63, v63, v78
	v_max3_f32 v68, v68, v62, v63
	v_add_f32_e32 v69, 0x41800000, v136
	v_cmp_gt_f32_e32 vcc, v68, v69
	s_cbranch_vccz .LBB0_456
	v_and_b32_e32 v70, 64, v228
	v_xor_b32_e32 v69, 16, v228
	v_add_u32_e32 v70, 64, v70
	v_cmp_lt_i32_e32 vcc, v69, v70
	s_nop 1
	v_cndmask_b32_e32 v69, v228, v69, vcc
	v_lshlrev_b32_e32 v69, 2, v69
	ds_bpermute_b32 v69, v69, v68
	v_max_f32_e32 v68, v68, v68
	s_waitcnt lgkmcnt(0)
	v_max_f32_e32 v69, v69, v69
	v_max_f32_e32 v68, v68, v69
	v_xor_b32_e32 v69, 32, v228
	v_cmp_lt_i32_e32 vcc, v69, v70
	s_nop 1
	v_cndmask_b32_e32 v69, v228, v69, vcc
	v_lshlrev_b32_e32 v69, 2, v69
	ds_bpermute_b32 v69, v69, v68
	s_waitcnt lgkmcnt(0)
	v_max3_f32 v69, v136, v68, v69
	v_sub_f32_e32 v68, v136, v69
	v_exp_f32_e32 v68, v68
	v_mov_b32_e32 v136, v69
	v_mul_f32_e32 v138, v138, v68
	v_pk_mul_f32 v[34:35], v[34:35], v[68:69] op_sel_hi:[1,0]
	v_pk_mul_f32 v[32:33], v[32:33], v[68:69] op_sel_hi:[1,0]
	v_pk_mul_f32 v[30:31], v[30:31], v[68:69] op_sel_hi:[1,0]
	v_pk_mul_f32 v[28:29], v[28:29], v[68:69] op_sel_hi:[1,0]
	v_pk_mul_f32 v[26:27], v[26:27], v[68:69] op_sel_hi:[1,0]
	v_pk_mul_f32 v[24:25], v[24:25], v[68:69] op_sel_hi:[1,0]
	v_pk_mul_f32 v[22:23], v[22:23], v[68:69] op_sel_hi:[1,0]
	v_pk_mul_f32 v[20:21], v[20:21], v[68:69] op_sel_hi:[1,0]

.LBB0_458:
	v_cvt_pk_bf16_f32 v52, v52, v53
	v_cvt_pk_bf16_f32 v53, v54, v55
	v_cvt_pk_bf16_f32 v54, v60, v61
	v_sub_f32_e32 v60, v67, v134
	v_exp_f32_e32 v68, v60
	v_sub_f32_e32 v60, v66, v134
	v_exp_f32_e32 v69, v60
	v_sub_f32_e32 v60, v65, v134
	v_sub_f32_e32 v57, v57, v134
	v_exp_f32_e32 v70, v60
	v_sub_f32_e32 v60, v64, v134
	v_sub_f32_e32 v59, v59, v134
	v_exp_f32_e32 v73, v57
	v_sub_f32_e32 v57, v58, v134
	v_sub_f32_e32 v56, v56, v134
	v_cvt_pk_bf16_f32 v55, v62, v63
	v_exp_f32_e32 v71, v60
	v_exp_f32_e32 v72, v59
	ds_read_b64_tr_b16 v[62:63], v158 offset:2560
	ds_read_b64_tr_b16 v[60:61], v158
	v_exp_f32_e32 v74, v57
	v_exp_f32_e32 v75, v56
	ds_read_b64_tr_b16 v[64:65], v158 offset:32
	ds_read_b64_tr_b16 v[66:67], v158 offset:2592
	v_cvt_pk_bf16_f32 v56, v68, v69
	v_cvt_pk_bf16_f32 v57, v70, v71
	v_cvt_pk_bf16_f32 v58, v72, v73
	v_cvt_pk_bf16_f32 v59, v74, v75
	s_waitcnt lgkmcnt(2)
	v_mfma_f32_16x16x32_bf16 v[32:35], v[60:63], v[52:55], v[32:35]
	v_add_f32_e32 v68, 0, v68
	v_add_f32_e32 v68, v69, v68
	v_add_f32_e32 v68, v70, v68
	v_mfma_f32_16x16x32_bf16 v[16:19], v[60:63], v[56:59], v[16:19]
	ds_read_b64_tr_b16 v[60:61], v158 offset:64
	s_andn2_b64 vcc, exec, s[24:25]
	s_mov_b64 s[24:25], -1
	s_waitcnt lgkmcnt(1)
	v_mfma_f32_16x16x32_bf16 v[28:31], v[64:67], v[52:55], v[28:31]
	v_mfma_f32_16x16x32_bf16 v[12:15], v[64:67], v[56:59], v[12:15]
	ds_read_b64_tr_b16 v[62:63], v158 offset:2624
	ds_read_b64_tr_b16 v[64:65], v158 offset:96
	ds_read_b64_tr_b16 v[66:67], v158 offset:2656
	s_waitcnt lgkmcnt(2)
	v_mfma_f32_16x16x32_bf16 v[24:27], v[60:63], v[52:55], v[24:27]
	v_mfma_f32_16x16x32_bf16 v[8:11], v[60:63], v[56:59], v[8:11]
	v_add_f32_e32 v60, v71, v68
	v_add_f32_e32 v60, v72, v60
	v_add_f32_e32 v60, v73, v60
	s_waitcnt lgkmcnt(0)
	v_mfma_f32_16x16x32_bf16 v[20:23], v[64:67], v[52:55], v[20:23]
	v_add_f32_e32 v52, v74, v60
	v_add_f32_e32 v52, v75, v52
	v_add_f32_e32 v1, v1, v52
	v_mfma_f32_16x16x32_bf16 v[4:7], v[64:67], v[56:59], v[4:7]
	s_cbranch_vccnz .LBB0_453
	s_cmp_ge_i32 s37, s36
	s_cselect_b64 s[24:25], -1, 0
	s_cmp_lt_i32 s37, s36
	s_cselect_b32 s38, s37, s38
	s_lshl_b32 s38, s38, 5
	s_sub_i32 s38, s35, s38
	s_cmp_lt_i32 s38, 0
	s_cbranch_scc1 .Latt_slow2
	s_add_i32 s98, s38, 31
	s_cmp_gt_i32 s98, s34
	s_cbranch_scc1 .Latt_slow2
	s_lshl_b32 s98, s38, s14
	s_add_i32 s98, s98, s21
	s_mulk_i32 s98, 0x1800
	s_mov_b32 s99, 0
	v_lshl_add_u64 v[52:53], s[98:99], 0, v[164:165]
	v_lshl_add_u64 v[60:61], s[98:99], 0, v[166:167]
	v_lshl_add_u64 v[68:69], s[98:99], 0, v[168:169]
	v_lshl_add_u64 v[76:77], s[98:99], 0, v[170:171]
	s_branch .Latt_join2
.Latt_slow2:
	v_or_b32_e32 v76, s38, v142
	v_min_i32_e32 v52, s34, v76
	v_or_b32_e32 v60, 8, v76
	v_or_b32_e32 v68, 16, v76
	v_or_b32_e32 v76, 24, v76
	v_min_i32_e32 v60, s34, v60
	v_min_i32_e32 v68, s34, v68
	v_min_i32_e32 v76, s34, v76
	v_max_i32_e32 v52, 0, v52
	v_max_i32_e32 v60, 0, v60
	v_max_i32_e32 v68, 0, v68
	v_max_i32_e32 v76, 0, v76
	v_lshlrev_b32_e32 v52, s14, v52
	v_lshlrev_b32_e32 v60, s14, v60
	v_lshlrev_b32_e32 v68, s14, v68
	v_lshlrev_b32_e32 v76, s14, v76
	v_add_u32_e32 v52, s21, v52
	v_add_u32_e32 v60, s21, v60
	v_add_u32_e32 v68, s21, v68
	v_add_u32_e32 v76, s21, v76
	v_mul_u32_u24_e32 v52, 0x1800, v52
	v_mul_u32_u24_e32 v60, 0x1800, v60
	v_mul_u32_u24_e32 v68, 0x1800, v68
	v_mul_u32_u24_e32 v76, 0x1800, v76
	v_ashrrev_i32_e32 v53, 31, v52
	v_ashrrev_i32_e32 v61, 31, v60
	v_ashrrev_i32_e32 v69, 31, v68
	v_ashrrev_i32_e32 v77, 31, v76
	v_lshl_add_u64 v[52:53], v[128:129], 0, v[52:53]
	v_lshl_add_u64 v[60:61], v[128:129], 0, v[60:61]
	v_lshl_add_u64 v[68:69], v[128:129], 0, v[68:69]
	v_lshl_add_u64 v[76:77], v[128:129], 0, v[76:77]
.Latt_join2:
	global_load_dwordx4 v[56:59], v[52:53], off offset:512
	s_nop 0
	global_load_dwordx4 v[52:55], v[52:53], off offset:1024
	s_nop 0
	global_load_dwordx4 v[64:67], v[60:61], off offset:512
	s_nop 0
	global_load_dwordx4 v[60:63], v[60:61], off offset:1024
	s_nop 0
	global_load_dwordx4 v[72:75], v[68:69], off offset:512
	s_nop 0
	global_load_dwordx4 v[68:71], v[68:69], off offset:1024
	s_nop 0
	global_load_dwordx4 v[80:83], v[76:77], off offset:512
	s_nop 0
	global_load_dwordx4 v[76:79], v[76:77], off offset:1024
	s_waitcnt vmcnt(15)
	ds_write_b128 v155, v[92:95]
	s_waitcnt vmcnt(13)
	ds_write_b128 v155, v[100:103] offset:1152
	s_waitcnt vmcnt(11)
	ds_write_b128 v155, v[108:111] offset:2304
	s_waitcnt vmcnt(9)
	ds_write_b128 v155, v[112:115] offset:3456
	ds_read_b128 v[92:95], v156 offset:2368
	ds_read_b128 v[100:103], v156 offset:2304
	ds_read_b128 v[108:111], v156 offset:64
	ds_read_b128 v[112:115], v156
	s_waitcnt lgkmcnt(0)
	ds_write_b128 v157, v[84:87]
	ds_write_b128 v157, v[88:91] offset:1280
	ds_write_b128 v157, v[96:99] offset:2560
	s_waitcnt vmcnt(8)
	ds_write_b128 v157, v[104:107] offset:3840
	v_mfma_f32_16x16x32_bf16 v[84:87], v[112:115], v[36:39], 0
	ds_read2_b32 v[96:97], v135 offset0:50 offset1:51
	ds_read2_b32 v[98:99], v135 offset0:48 offset1:49
	ds_read2_b32 v[104:105], v135 offset0:34 offset1:35
	ds_read2_b32 v[106:107], v135 offset0:32 offset1:33
	s_waitcnt lgkmcnt(0)
	v_mfma_f32_16x16x32_bf16 v[88:91], v[100:103], v[36:39], 0
	v_mfma_f32_16x16x32_bf16 v[84:87], v[108:111], v[40:43], v[84:87]
	v_mfma_f32_16x16x32_bf16 v[88:91], v[92:95], v[40:43], v[88:91]
	s_nop 6
	v_add_f32_e32 v84, v84, v97
	v_add_f32_e32 v85, v85, v96
	v_max3_f32 v96, v84, s28, v85
	v_add_f32_e32 v86, v86, v99
	v_add_f32_e32 v87, v87, v98
	v_max3_f32 v96, v96, v86, v87
	v_add_f32_e32 v88, v88, v105
	v_add_f32_e32 v89, v89, v104
	v_max3_f32 v96, v96, v88, v89
	v_add_f32_e32 v90, v90, v107
	v_add_f32_e32 v91, v91, v106
	v_max3_f32 v96, v96, v90, v91
	v_add_f32_e32 v97, 0x41800000, v136
	v_cmp_gt_f32_e32 vcc, v96, v97
	s_cbranch_vccz .LBB0_461
	v_and_b32_e32 v98, 64, v228
	v_xor_b32_e32 v97, 16, v228
	v_add_u32_e32 v98, 64, v98
	v_cmp_lt_i32_e32 vcc, v97, v98
	s_nop 1
	v_cndmask_b32_e32 v97, v228, v97, vcc
	v_lshlrev_b32_e32 v97, 2, v97
	ds_bpermute_b32 v97, v97, v96
	v_max_f32_e32 v96, v96, v96
	s_waitcnt lgkmcnt(0)
	v_max_f32_e32 v97, v97, v97
	v_max_f32_e32 v96, v96, v97
	v_xor_b32_e32 v97, 32, v228
	v_cmp_lt_i32_e32 vcc, v97, v98
	s_nop 1
	v_cndmask_b32_e32 v97, v228, v97, vcc
	v_lshlrev_b32_e32 v97, 2, v97
	ds_bpermute_b32 v97, v97, v96
	s_waitcnt lgkmcnt(0)
	v_max3_f32 v97, v136, v96, v97
	v_sub_f32_e32 v96, v136, v97
	v_exp_f32_e32 v96, v96
	v_mov_b32_e32 v136, v97
	v_mul_f32_e32 v138, v138, v96
	v_pk_mul_f32 v[34:35], v[34:35], v[96:97] op_sel_hi:[1,0]
	v_pk_mul_f32 v[32:33], v[32:33], v[96:97] op_sel_hi:[1,0]
	v_pk_mul_f32 v[30:31], v[30:31], v[96:97] op_sel_hi:[1,0]
	v_pk_mul_f32 v[28:29], v[28:29], v[96:97] op_sel_hi:[1,0]
	v_pk_mul_f32 v[26:27], v[26:27], v[96:97] op_sel_hi:[1,0]
	v_pk_mul_f32 v[24:25], v[24:25], v[96:97] op_sel_hi:[1,0]
	v_pk_mul_f32 v[22:23], v[22:23], v[96:97] op_sel_hi:[1,0]
	v_pk_mul_f32 v[20:21], v[20:21], v[96:97] op_sel_hi:[1,0]

.LBB0_1112:
	s_add_i32 s23, s35, 1
	s_cmp_ge_i32 s23, s22
	s_cselect_b64 s[20:21], -1, 0
	s_and_b64 s[24:25], s[20:21], exec
	s_cselect_b32 s25, 0, s23
	s_cmp_lg_u64 s[20:21], 0
	s_addc_u32 s37, s34, 0
	s_cmp_lt_i32 s37, 2
	s_cselect_b64 s[20:21], -1, 0
	s_cmp_gt_i32 s37, 1
	s_cselect_b32 s24, s34, s37
	s_cselect_b32 s49, s35, s25
	s_add_i32 s24, s24, s2
	s_add_i32 s23, s24, s31
	s_ashr_i32 s41, s23, 4
	s_and_b32 s40, s41, 0xffffffe0
	s_lshl_b32 s48, s49, 5
	s_sub_i32 s52, s40, s48
	s_cmp_lt_i32 s52, 0
	s_cbranch_scc1 .Latt0_slow1
	s_add_i32 s98, s52, 31
	s_add_i32 s99, s41, 15
	s_cmp_gt_i32 s98, s99
	s_cbranch_scc1 .Latt0_slow1
	s_lshl_b32 s98, s52, 4
	s_add_i32 s98, s98, s24
	s_mulk_i32 s98, 0x1800
	s_mov_b32 s99, 0
	v_lshl_add_u64 v[4:5], s[98:99], 0, v[174:175]
	global_load_dwordx4 v[78:81], v[4:5], off offset:512
	global_load_dwordx4 v[70:73], v[4:5], off offset:1024
	v_lshl_add_u64 v[4:5], s[98:99], 0, v[176:177]
	global_load_dwordx4 v[86:89], v[4:5], off offset:512
	global_load_dwordx4 v[74:77], v[4:5], off offset:1024
	v_lshl_add_u64 v[4:5], s[98:99], 0, v[178:179]
	global_load_dwordx4 v[94:97], v[4:5], off offset:512
	global_load_dwordx4 v[82:85], v[4:5], off offset:1024
	v_lshl_add_u64 v[4:5], s[98:99], 0, v[180:181]
	global_load_dwordx4 v[98:101], v[4:5], off offset:512
	global_load_dwordx4 v[90:93], v[4:5], off offset:1024
	s_add_i32 s52, s41, 15
	s_branch .Latt0_join1
.Latt0_slow1:
	v_or_b32_e32 v1, s52, v142
	s_add_i32 s52, s41, 15
	v_min_i32_e32 v3, s52, v1
	v_max_i32_e32 v3, 0, v3
	v_lshl_add_u32 v3, v3, 4, s24
	v_mul_u32_u24_e32 v4, 0x1800, v3
	v_or_b32_e32 v3, 8, v1
	v_min_i32_e32 v3, s52, v3
	v_ashrrev_i32_e32 v5, 31, v4
	v_max_i32_e32 v3, 0, v3
	v_lshl_add_u64 v[4:5], v[128:129], 0, v[4:5]
	v_lshl_add_u32 v3, v3, 4, s24
	global_load_dwordx4 v[78:81], v[4:5], off offset:512
	global_load_dwordx4 v[70:73], v[4:5], off offset:1024
	v_mul_u32_u24_e32 v4, 0x1800, v3
	v_or_b32_e32 v3, 16, v1
	v_min_i32_e32 v3, s52, v3
	v_ashrrev_i32_e32 v5, 31, v4
	v_max_i32_e32 v3, 0, v3
	v_lshl_add_u64 v[4:5], v[128:129], 0, v[4:5]
	v_lshl_add_u32 v3, v3, 4, s24
	v_or_b32_e32 v1, 24, v1
	global_load_dwordx4 v[86:89], v[4:5], off offset:512
	global_load_dwordx4 v[74:77], v[4:5], off offset:1024
	v_mul_u32_u24_e32 v4, 0x1800, v3
	v_min_i32_e32 v1, s52, v1
	v_ashrrev_i32_e32 v5, 31, v4
	v_max_i32_e32 v1, 0, v1
	v_lshl_add_u64 v[4:5], v[128:129], 0, v[4:5]
	v_lshl_add_u32 v1, v1, 4, s24
	global_load_dwordx4 v[94:97], v[4:5], off offset:512
	global_load_dwordx4 v[82:85], v[4:5], off offset:1024
	v_mul_u32_u24_e32 v4, 0x1800, v1
	v_ashrrev_i32_e32 v5, 31, v4
	v_lshl_add_u64 v[4:5], v[128:129], 0, v[4:5]
	global_load_dwordx4 v[98:101], v[4:5], off offset:512
	global_load_dwordx4 v[90:93], v[4:5], off offset:1024
.Latt0_join1:
	s_cmp_lg_u32 s49, 0
	s_cbranch_scc1 .LBB0_1114
	v_add_u32_e32 v1, s23, v144
	v_mad_i64_i32 v[4:5], s[52:53], v1, s27, v[126:127]
	global_load_dwordx4 v[6:9], v[4:5], off
	global_load_dwordx4 v[10:13], v[4:5], off offset:64

.LBB0_1122:
	s_andn2_b64 vcc, exec, s[20:21]
	s_mov_b64 s[20:21], -1
	s_cbranch_vccnz .LBB0_1111
	s_sub_i32 s20, 0x80, s40
	s_ashr_i32 s20, s20, 5
	s_sub_i32 s20, 5, s20
	s_cmpk_lt_i32 s40, 0x80
	s_cselect_b32 s49, s20, 5
	s_add_i32 s34, s25, 1
	s_cmp_ge_i32 s34, s49
	s_cselect_b64 s[20:21], -1, 0
	s_and_b64 s[22:23], s[20:21], exec
	s_cselect_b32 s35, 0, s34
	s_cmp_lg_u64 s[20:21], 0
	s_addc_u32 s34, s37, 0
	s_cmp_lt_i32 s34, 2
	s_cselect_b64 s[22:23], -1, 0
	s_cmp_gt_i32 s34, 1
	s_cselect_b64 s[20:21], -1, 0
	s_and_b64 s[38:39], s[20:21], exec
	s_cselect_b32 s36, s37, s34
	s_cselect_b32 s53, s25, s35
	s_add_i32 s36, s36, s2
	s_add_i32 s52, s36, s31
	s_ashr_i32 s38, s52, 4
	s_and_b32 s39, s38, 0xffffffe0
	s_lshl_b32 s54, s53, 5
	s_sub_i32 s54, s39, s54
	s_cmp_lt_i32 s54, 0
	s_cbranch_scc1 .Latt0_slow0
	s_add_i32 s98, s54, 31
	s_add_i32 s99, s38, 15
	s_cmp_gt_i32 s98, s99
	s_cbranch_scc1 .Latt0_slow0
	s_lshl_b32 s98, s54, 4
	s_add_i32 s98, s98, s36
	s_mulk_i32 s98, 0x1800
	s_mov_b32 s99, 0
	v_lshl_add_u64 v[4:5], s[98:99], 0, v[174:175]
	global_load_dwordx4 v[26:29], v[4:5], off offset:512
	global_load_dwordx4 v[22:25], v[4:5], off offset:1024
	v_lshl_add_u64 v[4:5], s[98:99], 0, v[176:177]
	global_load_dwordx4 v[34:37], v[4:5], off offset:512
	global_load_dwordx4 v[30:33], v[4:5], off offset:1024
	v_lshl_add_u64 v[4:5], s[98:99], 0, v[178:179]
	global_load_dwordx4 v[42:45], v[4:5], off offset:512
	global_load_dwordx4 v[38:41], v[4:5], off offset:1024
	v_lshl_add_u64 v[4:5], s[98:99], 0, v[180:181]
	global_load_dwordx4 v[50:53], v[4:5], off offset:512
	global_load_dwordx4 v[46:49], v[4:5], off offset:1024
	s_add_i32 s54, s38, 15
	s_branch .Latt0_join0
.Latt0_slow0:
	v_or_b32_e32 v1, s54, v142
	s_add_i32 s54, s38, 15
	v_min_i32_e32 v3, s54, v1
	v_max_i32_e32 v3, 0, v3
	v_lshl_add_u32 v3, v3, 4, s36
	v_mul_u32_u24_e32 v4, 0x1800, v3
	v_or_b32_e32 v3, 8, v1
	v_min_i32_e32 v3, s54, v3
	v_ashrrev_i32_e32 v5, 31, v4
	v_max_i32_e32 v3, 0, v3
	v_lshl_add_u64 v[4:5], v[128:129], 0, v[4:5]
	v_lshl_add_u32 v3, v3, 4, s36
	global_load_dwordx4 v[26:29], v[4:5], off offset:512
	global_load_dwordx4 v[22:25], v[4:5], off offset:1024
	v_mul_u32_u24_e32 v4, 0x1800, v3
	v_or_b32_e32 v3, 16, v1
	v_min_i32_e32 v3, s54, v3
	v_ashrrev_i32_e32 v5, 31, v4
	v_max_i32_e32 v3, 0, v3
	v_lshl_add_u64 v[4:5], v[128:129], 0, v[4:5]
	v_lshl_add_u32 v3, v3, 4, s36
	v_or_b32_e32 v1, 24, v1
	global_load_dwordx4 v[34:37], v[4:5], off offset:512
	global_load_dwordx4 v[30:33], v[4:5], off offset:1024
	v_mul_u32_u24_e32 v4, 0x1800, v3
	v_min_i32_e32 v1, s54, v1
	v_ashrrev_i32_e32 v5, 31, v4
	v_max_i32_e32 v1, 0, v1
	v_lshl_add_u64 v[4:5], v[128:129], 0, v[4:5]
	v_lshl_add_u32 v1, v1, 4, s36
	global_load_dwordx4 v[42:45], v[4:5], off offset:512
	global_load_dwordx4 v[38:41], v[4:5], off offset:1024
	v_mul_u32_u24_e32 v4, 0x1800, v1
	v_ashrrev_i32_e32 v5, 31, v4
	v_lshl_add_u64 v[4:5], v[128:129], 0, v[4:5]
	global_load_dwordx4 v[50:53], v[4:5], off offset:512
	global_load_dwordx4 v[46:49], v[4:5], off offset:1024
.Latt0_join0:
	s_cmp_lg_u32 s53, 0
	s_cbranch_scc1 .LBB0_1125
	v_add_u32_e32 v1, s52, v144
	v_mad_i64_i32 v[4:5], s[52:53], v1, s27, v[126:127]
	global_load_dwordx4 v[6:9], v[4:5], off
	global_load_dwordx4 v[10:13], v[4:5], off offset:64

.LBB0_1145:
	s_add_i32 s39, s37, -2
	s_add_i32 s38, s37, -1
	s_cmp_lt_i32 s38, s36
	s_cselect_b64 s[24:25], -1, 0
	s_and_b64 s[40:41], s[24:25], exec
	s_cselect_b32 s39, s38, s39
	s_lshl_b32 s39, s39, 5
	s_sub_i32 s39, s35, s39
	s_waitcnt vmcnt(0)
	s_cmp_lt_i32 s39, 0
	s_cbranch_scc1 .Latt_slow1
	s_add_i32 s98, s39, 31
	s_cmp_gt_i32 s98, s34
	s_cbranch_scc1 .Latt_slow1
	s_lshl_b32 s98, s39, s14
	s_add_i32 s98, s98, s21
	s_mulk_i32 s98, 0x1800
	s_mov_b32 s99, 0
	v_lshl_add_u64 v[84:85], s[98:99], 0, v[164:165]
	v_lshl_add_u64 v[88:89], s[98:99], 0, v[166:167]
	v_lshl_add_u64 v[96:97], s[98:99], 0, v[168:169]
	v_lshl_add_u64 v[104:105], s[98:99], 0, v[170:171]
	s_branch .Latt_join1

.Latt_join1:
	global_load_dwordx4 v[92:95], v[84:85], off offset:512
	s_nop 0
	global_load_dwordx4 v[84:87], v[84:85], off offset:1024
	s_nop 0
	global_load_dwordx4 v[100:103], v[88:89], off offset:512
	s_nop 0
	global_load_dwordx4 v[88:91], v[88:89], off offset:1024
	s_nop 0
	global_load_dwordx4 v[108:111], v[96:97], off offset:512
	s_nop 0
	global_load_dwordx4 v[96:99], v[96:97], off offset:1024
	s_nop 0
	global_load_dwordx4 v[112:115], v[104:105], off offset:512
	s_nop 0
	global_load_dwordx4 v[104:107], v[104:105], off offset:1024
	s_waitcnt vmcnt(15)
	ds_write_b128 v155, v[56:59]
	s_waitcnt vmcnt(13)
	ds_write_b128 v155, v[64:67] offset:1152
	s_waitcnt vmcnt(11)
	ds_write_b128 v155, v[72:75] offset:2304
	s_waitcnt vmcnt(9)
	ds_write_b128 v155, v[80:83] offset:3456
	ds_read_b128 v[56:59], v156 offset:2368
	ds_read_b128 v[64:67], v156 offset:2304
	ds_read_b128 v[72:75], v156 offset:64
	ds_read_b128 v[80:83], v156
	s_waitcnt lgkmcnt(0)
	s_nop 0
	v_mfma_f32_16x16x32_bf16 v[160:163], v[80:83], v[36:39], 0
	ds_write_b128 v157, v[52:55]
	ds_write_b128 v157, v[60:63] offset:1280
	ds_write_b128 v157, v[68:71] offset:2560
	s_waitcnt vmcnt(8)
	ds_write_b128 v157, v[76:79] offset:3840
	ds_read2_b32 v[68:69], v135 offset0:18 offset1:19
	ds_read2_b32 v[70:71], v135 offset1:1
	ds_read2_b32 v[76:77], v135 offset0:16 offset1:17
	ds_read2_b32 v[78:79], v135 offset0:2 offset1:3
	v_mfma_f32_16x16x32_bf16 v[52:55], v[64:67], v[36:39], 0
	v_mfma_f32_16x16x32_bf16 v[160:163], v[72:75], v[40:43], v[160:163]
	v_mfma_f32_16x16x32_bf16 v[60:63], v[56:59], v[40:43], v[52:55]
	s_waitcnt lgkmcnt(3)
	s_nop 4
	v_mov_b32_e32 v52, v69
	s_waitcnt lgkmcnt(2)
	v_mov_b32_e32 v69, v70
	s_waitcnt lgkmcnt(1)
	v_mov_b32_e32 v53, v77
	s_waitcnt lgkmcnt(0)
	v_mov_b32_e32 v70, v79
	s_nop 0
	v_add_f32_e32 v52, v160, v52
	v_add_f32_e32 v54, v161, v68
	v_max3_f32 v68, v52, s28, v54
	v_add_f32_e32 v53, v162, v53
	v_add_f32_e32 v55, v163, v76
	v_max3_f32 v68, v68, v53, v55
	v_add_f32_e32 v60, v60, v70
	v_add_f32_e32 v61, v61, v78
	v_max3_f32 v68, v68, v60, v61
	v_add_f32_e32 v62, v62, v71
	v_add_f32_e32 v63, v63, v69
	v_max3_f32 v68, v68, v62, v63
	v_add_f32_e32 v69, 0x41800000, v136
	v_cmp_gt_f32_e32 vcc, v68, v69
	s_cbranch_vccz .LBB0_1147
	v_and_b32_e32 v70, 64, v228
	v_xor_b32_e32 v69, 16, v228
	v_add_u32_e32 v70, 64, v70
	v_cmp_lt_i32_e32 vcc, v69, v70
	v_xor_b32_e32 v71, 32, v228
	s_nop 0
	v_cndmask_b32_e32 v69, v228, v69, vcc
	v_lshlrev_b32_e32 v69, 2, v69
	ds_bpermute_b32 v69, v69, v68
	v_max_f32_e32 v68, v68, v68
	v_cmp_lt_i32_e32 vcc, v71, v70
	s_waitcnt lgkmcnt(0)
	v_max_f32_e32 v69, v69, v69
	v_max_f32_e32 v68, v68, v69
	v_cndmask_b32_e32 v69, v228, v71, vcc
	v_lshlrev_b32_e32 v69, 2, v69
	ds_bpermute_b32 v69, v69, v68
	s_waitcnt lgkmcnt(0)
	v_max3_f32 v69, v136, v68, v69
	v_sub_f32_e32 v68, v136, v69
	v_exp_f32_e32 v68, v68
	v_mov_b32_e32 v136, v69
	v_mul_f32_e32 v138, v138, v68
	v_pk_mul_f32 v[34:35], v[34:35], v[68:69] op_sel_hi:[1,0]
	v_pk_mul_f32 v[32:33], v[32:33], v[68:69] op_sel_hi:[1,0]
	v_pk_mul_f32 v[30:31], v[30:31], v[68:69] op_sel_hi:[1,0]
	v_pk_mul_f32 v[28:29], v[28:29], v[68:69] op_sel_hi:[1,0]
	v_pk_mul_f32 v[26:27], v[26:27], v[68:69] op_sel_hi:[1,0]
	v_pk_mul_f32 v[24:25], v[24:25], v[68:69] op_sel_hi:[1,0]
	v_pk_mul_f32 v[22:23], v[22:23], v[68:69] op_sel_hi:[1,0]
	v_pk_mul_f32 v[20:21], v[20:21], v[68:69] op_sel_hi:[1,0]

.LBB0_1149:
	v_cvt_pk_bf16_f32 v52, v52, v53
	v_cvt_pk_bf16_f32 v53, v54, v55
	v_cvt_pk_bf16_f32 v54, v60, v61
	v_sub_f32_e32 v60, v67, v134
	v_exp_f32_e32 v76, v60
	v_sub_f32_e32 v60, v66, v134
	v_exp_f32_e32 v77, v60
	v_sub_f32_e32 v60, v65, v134
	v_exp_f32_e32 v78, v60
	v_sub_f32_e32 v60, v64, v134
	v_exp_f32_e32 v79, v60
	v_sub_f32_e32 v59, v59, v134
	v_sub_f32_e32 v58, v58, v134
	v_sub_f32_e32 v57, v57, v134
	v_sub_f32_e32 v60, v56, v134
	v_exp_f32_e32 v80, v59
	v_exp_f32_e32 v81, v58
	v_exp_f32_e32 v82, v57
	ds_read_b64_tr_b16 v[58:59], v158 offset:2560
	ds_read_b64_tr_b16 v[56:57], v158
	v_exp_f32_e32 v83, v60
	v_cvt_pk_bf16_f32 v55, v62, v63
	v_cvt_pk_bf16_f32 v60, v76, v77
	v_cvt_pk_bf16_f32 v61, v78, v79
	v_cvt_pk_bf16_f32 v62, v80, v81
	v_cvt_pk_bf16_f32 v63, v82, v83
	ds_read_b64_tr_b16 v[64:65], v158 offset:32
	ds_read_b64_tr_b16 v[68:69], v158 offset:64
	ds_read_b64_tr_b16 v[72:73], v158 offset:96
	ds_read_b64_tr_b16 v[66:67], v158 offset:2592
	ds_read_b64_tr_b16 v[70:71], v158 offset:2624
	ds_read_b64_tr_b16 v[74:75], v158 offset:2656
	s_waitcnt lgkmcnt(6)
	v_mfma_f32_16x16x32_bf16 v[32:35], v[56:59], v[52:55], v[32:35]
	s_andn2_b64 vcc, exec, s[24:25]
	s_mov_b64 s[24:25], -1
	v_mfma_f32_16x16x32_bf16 v[16:19], v[56:59], v[60:63], v[16:19]
	v_add_f32_e32 v56, 0, v76
	v_add_f32_e32 v56, v77, v56
	v_add_f32_e32 v56, v78, v56
	v_add_f32_e32 v56, v79, v56
	v_add_f32_e32 v56, v80, v56
	s_waitcnt lgkmcnt(2)
	v_mfma_f32_16x16x32_bf16 v[28:31], v[64:67], v[52:55], v[28:31]
	v_add_f32_e32 v56, v81, v56
	v_mfma_f32_16x16x32_bf16 v[12:15], v[64:67], v[60:63], v[12:15]
	s_waitcnt lgkmcnt(1)
	v_mfma_f32_16x16x32_bf16 v[24:27], v[68:71], v[52:55], v[24:27]
	v_mfma_f32_16x16x32_bf16 v[8:11], v[68:71], v[60:63], v[8:11]
	s_waitcnt lgkmcnt(0)
	v_mfma_f32_16x16x32_bf16 v[20:23], v[72:75], v[52:55], v[20:23]
	v_add_f32_e32 v52, v82, v56
	v_add_f32_e32 v52, v83, v52
	v_add_f32_e32 v1, v1, v52
	v_mfma_f32_16x16x32_bf16 v[4:7], v[72:75], v[60:63], v[4:7]
	s_cbranch_vccnz .LBB0_1144
	s_cmp_ge_i32 s37, s36
	s_cselect_b64 s[24:25], -1, 0
	s_cmp_lt_i32 s37, s36
	s_cselect_b32 s38, s37, s38
	s_lshl_b32 s38, s38, 5
	s_sub_i32 s38, s35, s38
	s_cmp_lt_i32 s38, 0
	s_cbranch_scc1 .Latt_slow0
	s_add_i32 s98, s38, 31
	s_cmp_gt_i32 s98, s34
	s_cbranch_scc1 .Latt_slow0
	s_lshl_b32 s98, s38, s14
	s_add_i32 s98, s98, s21
	s_mulk_i32 s98, 0x1800
	s_mov_b32 s99, 0
	v_lshl_add_u64 v[52:53], s[98:99], 0, v[164:165]
	v_lshl_add_u64 v[60:61], s[98:99], 0, v[166:167]
	v_lshl_add_u64 v[68:69], s[98:99], 0, v[168:169]
	v_lshl_add_u64 v[76:77], s[98:99], 0, v[170:171]
	s_branch .Latt_join0

.Latt_join0:
	global_load_dwordx4 v[56:59], v[52:53], off offset:512
	s_nop 0
	global_load_dwordx4 v[52:55], v[52:53], off offset:1024
	s_nop 0
	global_load_dwordx4 v[64:67], v[60:61], off offset:512
	s_nop 0
	global_load_dwordx4 v[60:63], v[60:61], off offset:1024
	s_nop 0
	global_load_dwordx4 v[72:75], v[68:69], off offset:512
	s_nop 0
	global_load_dwordx4 v[68:71], v[68:69], off offset:1024
	s_nop 0
	global_load_dwordx4 v[80:83], v[76:77], off offset:512
	s_nop 0
	global_load_dwordx4 v[76:79], v[76:77], off offset:1024
	s_waitcnt vmcnt(15)
	ds_write_b128 v155, v[92:95]
	s_waitcnt vmcnt(13)
	ds_write_b128 v155, v[100:103] offset:1152
	s_waitcnt vmcnt(11)
	ds_write_b128 v155, v[108:111] offset:2304
	s_waitcnt vmcnt(9)
	ds_write_b128 v155, v[112:115] offset:3456
	ds_read_b128 v[92:95], v156 offset:2368
	ds_read_b128 v[100:103], v156 offset:2304
	ds_read_b128 v[108:111], v156 offset:64
	ds_read_b128 v[112:115], v156
	s_waitcnt lgkmcnt(0)
	s_nop 0
	v_mfma_f32_16x16x32_bf16 v[160:163], v[112:115], v[36:39], 0
	ds_write_b128 v157, v[84:87]
	ds_write_b128 v157, v[88:91] offset:1280
	ds_write_b128 v157, v[96:99] offset:2560
	s_waitcnt vmcnt(8)
	ds_write_b128 v157, v[104:107] offset:3840
	ds_read2_b32 v[96:97], v135 offset0:50 offset1:51
	ds_read2_b32 v[98:99], v135 offset0:32 offset1:33
	ds_read2_b32 v[104:105], v135 offset0:48 offset1:49
	ds_read2_b32 v[106:107], v135 offset0:34 offset1:35
	v_mfma_f32_16x16x32_bf16 v[88:91], v[100:103], v[36:39], 0
	s_waitcnt lgkmcnt(0)
	v_mfma_f32_16x16x32_bf16 v[84:87], v[108:111], v[40:43], v[160:163]
	v_mfma_f32_16x16x32_bf16 v[88:91], v[92:95], v[40:43], v[88:91]
	s_nop 6
	v_add_f32_e32 v84, v84, v97
	v_add_f32_e32 v85, v85, v96
	v_max3_f32 v96, v84, s28, v85
	v_add_f32_e32 v86, v86, v105
	v_add_f32_e32 v87, v87, v104
	v_max3_f32 v96, v96, v86, v87
	v_add_f32_e32 v88, v88, v107
	v_add_f32_e32 v89, v89, v106
	v_max3_f32 v96, v96, v88, v89
	v_add_f32_e32 v90, v90, v99
	v_add_f32_e32 v91, v91, v98
	v_max3_f32 v96, v96, v90, v91
	v_add_f32_e32 v97, 0x41800000, v136
	v_cmp_gt_f32_e32 vcc, v96, v97
	s_cbranch_vccz .LBB0_1152
	v_and_b32_e32 v98, 64, v228
	v_xor_b32_e32 v97, 16, v228
	v_add_u32_e32 v98, 64, v98
	v_cmp_lt_i32_e32 vcc, v97, v98
	v_xor_b32_e32 v99, 32, v228
	s_nop 0
	v_cndmask_b32_e32 v97, v228, v97, vcc
	v_lshlrev_b32_e32 v97, 2, v97
	ds_bpermute_b32 v97, v97, v96
	v_max_f32_e32 v96, v96, v96
	v_cmp_lt_i32_e32 vcc, v99, v98
	s_waitcnt lgkmcnt(0)
	v_max_f32_e32 v97, v97, v97
	v_max_f32_e32 v96, v96, v97
	v_cndmask_b32_e32 v97, v228, v99, vcc
	v_lshlrev_b32_e32 v97, 2, v97
	ds_bpermute_b32 v97, v97, v96
	s_waitcnt lgkmcnt(0)
	v_max3_f32 v97, v136, v96, v97
	v_sub_f32_e32 v96, v136, v97
	v_exp_f32_e32 v96, v96
	v_mov_b32_e32 v136, v97
	v_mul_f32_e32 v138, v138, v96
	v_pk_mul_f32 v[34:35], v[34:35], v[96:97] op_sel_hi:[1,0]
	v_pk_mul_f32 v[32:33], v[32:33], v[96:97] op_sel_hi:[1,0]
	v_pk_mul_f32 v[30:31], v[30:31], v[96:97] op_sel_hi:[1,0]
	v_pk_mul_f32 v[28:29], v[28:29], v[96:97] op_sel_hi:[1,0]
	v_pk_mul_f32 v[26:27], v[26:27], v[96:97] op_sel_hi:[1,0]
	v_pk_mul_f32 v[24:25], v[24:25], v[96:97] op_sel_hi:[1,0]
	v_pk_mul_f32 v[22:23], v[22:23], v[96:97] op_sel_hi:[1,0]
	v_pk_mul_f32 v[20:21], v[20:21], v[96:97] op_sel_hi:[1,0]

; __global__ void __launch_bounds__(NTHR, 2) hybrid_fwd(Args args) {
	.amdhsa_kernel _Z10hybrid_fwd4Args
		.amdhsa_group_segment_fixed_size 0
		.amdhsa_private_segment_fixed_size 0
		.amdhsa_kernarg_size 432
		.amdhsa_user_sgpr_count 2
		.amdhsa_user_sgpr_dispatch_ptr 0
		.amdhsa_user_sgpr_queue_ptr 0
		.amdhsa_user_sgpr_kernarg_segment_ptr 1
		.amdhsa_user_sgpr_dispatch_id 0
		.amdhsa_user_sgpr_kernarg_preload_length 0
		.amdhsa_user_sgpr_kernarg_preload_offset 0
		.amdhsa_user_sgpr_private_segment_size 0
		.amdhsa_uses_dynamic_stack 0
		.amdhsa_enable_private_segment 0
		.amdhsa_system_sgpr_workgroup_id_x 1
		.amdhsa_system_sgpr_workgroup_id_y 0
		.amdhsa_system_sgpr_workgroup_id_z 0
		.amdhsa_system_sgpr_workgroup_info 0
		.amdhsa_system_vgpr_workitem_id 0
		.amdhsa_next_free_vgpr 256
		.amdhsa_next_free_sgpr 100
		.amdhsa_accum_offset 256
		.amdhsa_reserve_vcc 1
		.amdhsa_float_round_mode_32 0
		.amdhsa_float_round_mode_16_64 0
		.amdhsa_float_denorm_mode_32 3
		.amdhsa_float_denorm_mode_16_64 3
		.amdhsa_dx10_clamp 1
		.amdhsa_ieee_mode 1
		.amdhsa_fp16_overflow 0
		.amdhsa_tg_split 0
		.amdhsa_exception_fp_ieee_invalid_op 0
		.amdhsa_exception_fp_denorm_src 0
		.amdhsa_exception_fp_ieee_div_zero 0
		.amdhsa_exception_fp_ieee_overflow 0
		.amdhsa_exception_fp_ieee_underflow 0
		.amdhsa_exception_fp_ieee_inexact 0
		.amdhsa_exception_int_div_zero 0
	.end_amdhsa_kernel

; __global__ void __launch_bounds__(NTHR, 2) hybrid_fwd(Args args) {
amdhsa.kernels:
  - .agpr_count:     0
    .args:
      - .offset:         0
        .size:           176
        .value_kind:     by_value
      - .offset:         176
        .size:           4
        .value_kind:     hidden_block_count_x
      - .offset:         180
        .size:           4
        .value_kind:     hidden_block_count_y
      - .offset:         184
        .size:           4
        .value_kind:     hidden_block_count_z
      - .offset:         188
        .size:           2
        .value_kind:     hidden_group_size_x
      - .offset:         190
        .size:           2
        .value_kind:     hidden_group_size_y
      - .offset:         192
        .size:           2
        .value_kind:     hidden_group_size_z
      - .offset:         194
        .size:           2
        .value_kind:     hidden_remainder_x
      - .offset:         196
        .size:           2
        .value_kind:     hidden_remainder_y
      - .offset:         198
        .size:           2
        .value_kind:     hidden_remainder_z
      - .offset:         216
        .size:           8
        .value_kind:     hidden_global_offset_x
      - .offset:         224
        .size:           8
        .value_kind:     hidden_global_offset_y
      - .offset:         232
        .size:           8
        .value_kind:     hidden_global_offset_z
      - .offset:         240
        .size:           2
        .value_kind:     hidden_grid_dims
      - .offset:         296
        .size:           4
        .value_kind:     hidden_dynamic_lds_size
    .group_segment_fixed_size: 0
    .kernarg_segment_align: 8
    .kernarg_segment_size: 432
    .language:       OpenCL C
    .language_version:
      - 2
      - 0
    .max_flat_workgroup_size: 512
    .name:           _Z10hybrid_fwd4Args
    .private_segment_fixed_size: 0
    .sgpr_count:     106
    .sgpr_spill_count: 95
    .symbol:         _Z10hybrid_fwd4Args.kd
    .uniform_work_group_size: 1
    .uses_dynamic_stack: false
    .vgpr_count:     256
    .vgpr_spill_count: 0
    .wavefront_size: 64
